# P2 K-loop: leading half (wr==0) skips the pre-barrier lgkmcnt(0); post-barrier wait covers WAR
# speedup vs baseline: 1.0008x; 1.0008x over previous
.LBB0_238:
	ds_read_b128 v[20:23], v203
	ds_read_b128 v[34:37], v203 offset:1024
	ds_read_b128 v[38:41], v203 offset:2048
	ds_read_b128 v[208:211], v203 offset:3072
	ds_read_b128 v[212:215], v207
	ds_read_b128 v[216:219], v207 offset:1024
	ds_read_b128 v[226:229], v207 offset:2048
	ds_read_b128 v[230:233], v207 offset:3072
	s_add_u32 s28, s10, 0xfffc0080
	s_addc_u32 s29, s11, -1
	s_cmp_eq_u32 s39, 12
	s_cselect_b32 s49, s2, s29
	s_cselect_b32 s48, s3, s28
	s_cselect_b32 s47, s13, s33
	s_cselect_b32 s46, s15, s20
	v_lshl_add_u64 v[24:25], s[10:11], 0, v[174:175]
	s_add_i32 m0, s58, 0xc000
	ds_read_b128 v[234:237], v224
	ds_read_b128 v[238:241], v224 offset:1024
	ds_read_b128 v[242:245], v224 offset:2048
	ds_read_b128 v[246:249], v224 offset:3072
	ds_read_b128 v[250:253], v224 offset:4096
	ds_read_b128 v[220:223], v224 offset:5120
	ds_read_b128 v[178:181], v224 offset:6144
	ds_read_b128 v[196:199], v224 offset:7168
	global_load_lds_dwordx4 v[24:25], off
	v_lshl_add_u64 v[24:25], s[10:11], 0, v[176:177]
	s_add_i32 m0, s58, 0xe000
	s_nop 0
	global_load_lds_dwordx4 v[24:25], off
	s_waitcnt vmcnt(8)
	s_and_b64 vcc, exec, s[26:27]
	s_cbranch_vccnz .Lnl_1
	s_waitcnt lgkmcnt(0)
.Lnl_1:
	s_barrier
	s_setprio 1
	s_waitcnt lgkmcnt(0)
	v_mfma_i32_16x16x64_i8 v[142:145], v[20:23], v[234:237], v[142:145]
	v_mfma_i32_16x16x64_i8 v[138:141], v[38:41], v[234:237], v[138:141]
	v_mfma_i32_16x16x64_i8 v[126:129], v[20:23], v[242:245], v[126:129]
	v_mfma_i32_16x16x64_i8 v[122:125], v[38:41], v[242:245], v[122:125]
	v_mfma_i32_16x16x64_i8 v[110:113], v[20:23], v[250:253], v[110:113]
	v_mfma_i32_16x16x64_i8 v[106:109], v[38:41], v[250:253], v[106:109]
	v_mfma_i32_16x16x64_i8 v[94:97], v[20:23], v[178:181], v[94:97]
	v_mfma_i32_16x16x64_i8 v[90:93], v[38:41], v[178:181], v[90:93]
	v_mfma_i32_16x16x64_i8 v[142:145], v[34:37], v[238:241], v[142:145]
	v_mfma_i32_16x16x64_i8 v[138:141], v[208:211], v[238:241], v[138:141]
	v_mfma_i32_16x16x64_i8 v[126:129], v[34:37], v[246:249], v[126:129]
	v_mfma_i32_16x16x64_i8 v[122:125], v[208:211], v[246:249], v[122:125]
	v_mfma_i32_16x16x64_i8 v[110:113], v[34:37], v[220:223], v[110:113]
	v_mfma_i32_16x16x64_i8 v[106:109], v[208:211], v[220:223], v[106:109]
	v_mfma_i32_16x16x64_i8 v[94:97], v[34:37], v[196:199], v[94:97]
	v_mfma_i32_16x16x64_i8 v[90:93], v[208:211], v[196:199], v[90:93]
	s_setprio 0
	s_setprio 1
	v_mfma_i32_16x16x64_i8 v[134:137], v[212:215], v[234:237], v[134:137]
	v_mfma_i32_16x16x64_i8 v[130:133], v[226:229], v[234:237], v[130:133]
	v_mfma_i32_16x16x64_i8 v[118:121], v[212:215], v[242:245], v[118:121]
	v_mfma_i32_16x16x64_i8 v[114:117], v[226:229], v[242:245], v[114:117]
	v_mfma_i32_16x16x64_i8 v[102:105], v[212:215], v[250:253], v[102:105]
	v_mfma_i32_16x16x64_i8 v[98:101], v[226:229], v[250:253], v[98:101]
	v_mfma_i32_16x16x64_i8 v[86:89], v[212:215], v[178:181], v[86:89]
	v_mfma_i32_16x16x64_i8 v[82:85], v[226:229], v[178:181], v[82:85]
	v_mfma_i32_16x16x64_i8 v[134:137], v[216:219], v[238:241], v[134:137]
	v_mfma_i32_16x16x64_i8 v[130:133], v[230:233], v[238:241], v[130:133]
	v_mfma_i32_16x16x64_i8 v[118:121], v[216:219], v[246:249], v[118:121]
	v_mfma_i32_16x16x64_i8 v[114:117], v[230:233], v[246:249], v[114:117]
	v_mfma_i32_16x16x64_i8 v[102:105], v[216:219], v[220:223], v[102:105]
	v_mfma_i32_16x16x64_i8 v[98:101], v[230:233], v[220:223], v[98:101]
	v_mfma_i32_16x16x64_i8 v[86:89], v[216:219], v[196:199], v[86:89]
	v_mfma_i32_16x16x64_i8 v[82:85], v[230:233], v[196:199], v[82:85]
	s_setprio 0
	s_barrier
	s_add_i32 s28, s80, s57
	v_lshl_add_u64 v[184:185], s[46:47], 0, v[148:149]
	s_mov_b32 m0, s28
	ds_read_b128 v[178:181], v224 offset:16384
	ds_read_b128 v[196:199], v224 offset:17408
	ds_read_b128 v[220:223], v224 offset:18432
	ds_read_b128 v[234:237], v224 offset:19456
	ds_read_b128 v[238:241], v224 offset:20480
	ds_read_b128 v[242:245], v224 offset:21504
	ds_read_b128 v[246:249], v224 offset:22528
	ds_read_b128 v[250:253], v224 offset:23552
	global_load_lds_dwordx4 v[184:185], off
	s_add_i32 m0, s28, 0x2000
	s_add_u32 s28, s46, 0x40000
	v_lshl_add_u64 v[188:189], s[46:47], 0, v[152:153]
	s_addc_u32 s29, s47, 0
	s_add_i32 s41, s81, s57
	global_load_lds_dwordx4 v[188:189], off
	v_lshl_add_u64 v[24:25], s[28:29], 0, v[148:149]
	s_mov_b32 m0, s41
	v_lshl_add_u64 v[192:193], s[48:49], 0, v[146:147]
	global_load_lds_dwordx4 v[24:25], off
	v_lshl_add_u64 v[24:25], s[28:29], 0, v[152:153]
	s_add_i32 m0, s41, 0x2000
	v_lshl_add_u64 v[200:201], s[48:49], 0, v[150:151]
	global_load_lds_dwordx4 v[24:25], off
	s_mov_b32 m0, s58
	s_nop 0
	global_load_lds_dwordx4 v[192:193], off
	s_mov_b32 m0, s59
	s_nop 0
	global_load_lds_dwordx4 v[200:201], off
	s_waitcnt vmcnt(8)
	s_and_b64 vcc, exec, s[26:27]
	s_cbranch_vccnz .Lnl_2
	s_waitcnt lgkmcnt(0)
.Lnl_2:
	s_barrier
	s_setprio 1
	s_waitcnt lgkmcnt(0)
	v_mfma_i32_16x16x64_i8 v[78:81], v[20:23], v[178:181], v[78:81]
	v_mfma_i32_16x16x64_i8 v[74:77], v[38:41], v[178:181], v[74:77]
	v_mfma_i32_16x16x64_i8 v[62:65], v[20:23], v[220:223], v[62:65]
	v_mfma_i32_16x16x64_i8 v[58:61], v[38:41], v[220:223], v[58:61]
	v_mfma_i32_16x16x64_i8 v[46:49], v[20:23], v[238:241], v[46:49]
	v_mfma_i32_16x16x64_i8 v[42:45], v[38:41], v[238:241], v[42:45]
	v_mfma_i32_16x16x64_i8 v[14:17], v[20:23], v[246:249], v[14:17]
	v_mfma_i32_16x16x64_i8 v[10:13], v[38:41], v[246:249], v[10:13]
	v_mfma_i32_16x16x64_i8 v[78:81], v[34:37], v[196:199], v[78:81]
	v_mfma_i32_16x16x64_i8 v[74:77], v[208:211], v[196:199], v[74:77]
	v_mfma_i32_16x16x64_i8 v[62:65], v[34:37], v[234:237], v[62:65]
	v_mfma_i32_16x16x64_i8 v[58:61], v[208:211], v[234:237], v[58:61]
	v_mfma_i32_16x16x64_i8 v[46:49], v[34:37], v[242:245], v[46:49]
	v_mfma_i32_16x16x64_i8 v[42:45], v[208:211], v[242:245], v[42:45]
	v_mfma_i32_16x16x64_i8 v[14:17], v[34:37], v[250:253], v[14:17]
	v_mfma_i32_16x16x64_i8 v[10:13], v[208:211], v[250:253], v[10:13]
	s_setprio 0
	s_setprio 1
	v_mfma_i32_16x16x64_i8 v[50:53], v[226:229], v[220:223], v[50:53]
	v_mfma_i32_16x16x64_i8 v[30:33], v[212:215], v[238:241], v[30:33]
	v_mfma_i32_16x16x64_i8 v[24:27], v[226:229], v[238:241], v[26:29]
	v_mfma_i32_16x16x64_i8 v[6:9], v[212:215], v[246:249], v[6:9]
	v_mfma_i32_16x16x64_i8 v[2:5], v[226:229], v[246:249], v[2:5]
	v_mfma_i32_16x16x64_i8 v[20:23], v[212:215], v[178:181], v[70:73]
	v_mfma_i32_16x16x64_i8 v[34:37], v[226:229], v[178:181], v[66:69]
	v_mfma_i32_16x16x64_i8 v[38:41], v[212:215], v[220:223], v[54:57]
	v_mfma_i32_16x16x64_i8 v[50:53], v[230:233], v[234:237], v[50:53]
	v_mfma_i32_16x16x64_i8 v[30:33], v[216:219], v[242:245], v[30:33]
	v_mfma_i32_16x16x64_i8 v[24:27], v[230:233], v[242:245], v[24:27]
	v_mfma_i32_16x16x64_i8 v[6:9], v[216:219], v[250:253], v[6:9]
	v_mfma_i32_16x16x64_i8 v[2:5], v[230:233], v[250:253], v[2:5]
	v_mfma_i32_16x16x64_i8 v[20:23], v[216:219], v[196:199], v[20:23]
	v_mfma_i32_16x16x64_i8 v[34:37], v[230:233], v[196:199], v[34:37]
	v_mfma_i32_16x16x64_i8 v[38:41], v[216:219], v[234:237], v[38:41]
	s_setprio 0
	s_barrier
	s_add_i32 s41, 0, 0x18000
	v_add_u32_e32 v28, s41, v183
	s_add_i32 s50, 0, 0x1c000
	ds_read_b128 v[54:57], v28
	ds_read_b128 v[66:69], v28 offset:1024
	ds_read_b128 v[70:73], v28 offset:2048
	ds_read_b128 v[178:181], v28 offset:3072
	v_add_u32_e32 v28, s50, v183
	ds_read_b128 v[196:199], v28
	ds_read_b128 v[208:211], v28 offset:1024
	ds_read_b128 v[212:215], v28 offset:2048
	ds_read_b128 v[216:219], v28 offset:3072
	s_add_u32 s28, s48, 0x40000
	s_addc_u32 s29, s49, 0
	s_mov_b32 m0, s60
	v_lshl_add_u64 v[28:29], s[28:29], 0, v[146:147]
	ds_read_b128 v[220:223], v224 offset:32768
	ds_read_b128 v[226:229], v224 offset:33792
	ds_read_b128 v[230:233], v224 offset:34816
	ds_read_b128 v[234:237], v224 offset:35840
	ds_read_b128 v[238:241], v224 offset:36864
	ds_read_b128 v[242:245], v224 offset:37888
	ds_read_b128 v[246:249], v224 offset:38912
	ds_read_b128 v[250:253], v224 offset:39936
	global_load_lds_dwordx4 v[28:29], off
	v_lshl_add_u64 v[28:29], s[28:29], 0, v[150:151]
	s_mov_b32 m0, s61
	s_nop 0
	global_load_lds_dwordx4 v[28:29], off
	s_waitcnt vmcnt(8)
	s_and_b64 vcc, exec, s[26:27]
	s_cbranch_vccnz .Lnl_3
	s_waitcnt lgkmcnt(0)
.Lnl_3:
	s_barrier
	s_setprio 1
	s_waitcnt lgkmcnt(0)
	v_mfma_i32_16x16x64_i8 v[142:145], v[54:57], v[220:223], v[142:145]
	v_mfma_i32_16x16x64_i8 v[138:141], v[70:73], v[220:223], v[138:141]
	v_mfma_i32_16x16x64_i8 v[126:129], v[54:57], v[230:233], v[126:129]
	v_mfma_i32_16x16x64_i8 v[122:125], v[70:73], v[230:233], v[122:125]
	v_mfma_i32_16x16x64_i8 v[110:113], v[54:57], v[238:241], v[110:113]
	v_mfma_i32_16x16x64_i8 v[106:109], v[70:73], v[238:241], v[106:109]
	v_mfma_i32_16x16x64_i8 v[94:97], v[54:57], v[246:249], v[94:97]
	v_mfma_i32_16x16x64_i8 v[90:93], v[70:73], v[246:249], v[90:93]
	v_mfma_i32_16x16x64_i8 v[142:145], v[66:69], v[226:229], v[142:145]
	v_mfma_i32_16x16x64_i8 v[138:141], v[178:181], v[226:229], v[138:141]
	v_mfma_i32_16x16x64_i8 v[126:129], v[66:69], v[234:237], v[126:129]
	v_mfma_i32_16x16x64_i8 v[122:125], v[178:181], v[234:237], v[122:125]
	v_mfma_i32_16x16x64_i8 v[110:113], v[66:69], v[242:245], v[110:113]
	v_mfma_i32_16x16x64_i8 v[106:109], v[178:181], v[242:245], v[106:109]
	v_mfma_i32_16x16x64_i8 v[94:97], v[66:69], v[250:253], v[94:97]
	v_mfma_i32_16x16x64_i8 v[90:93], v[178:181], v[250:253], v[90:93]
	s_setprio 0
	s_setprio 1
	v_mfma_i32_16x16x64_i8 v[134:137], v[196:199], v[220:223], v[134:137]
	v_mfma_i32_16x16x64_i8 v[130:133], v[212:215], v[220:223], v[130:133]
	v_mfma_i32_16x16x64_i8 v[118:121], v[196:199], v[230:233], v[118:121]
	v_mfma_i32_16x16x64_i8 v[114:117], v[212:215], v[230:233], v[114:117]
	v_mfma_i32_16x16x64_i8 v[102:105], v[196:199], v[238:241], v[102:105]
	v_mfma_i32_16x16x64_i8 v[98:101], v[212:215], v[238:241], v[98:101]
	v_mfma_i32_16x16x64_i8 v[86:89], v[196:199], v[246:249], v[86:89]
	v_mfma_i32_16x16x64_i8 v[82:85], v[212:215], v[246:249], v[82:85]
	v_mfma_i32_16x16x64_i8 v[134:137], v[208:211], v[226:229], v[134:137]
	v_mfma_i32_16x16x64_i8 v[130:133], v[216:219], v[226:229], v[130:133]
	v_mfma_i32_16x16x64_i8 v[118:121], v[208:211], v[234:237], v[118:121]
	v_mfma_i32_16x16x64_i8 v[114:117], v[216:219], v[234:237], v[114:117]
	v_mfma_i32_16x16x64_i8 v[102:105], v[208:211], v[242:245], v[102:105]
	v_mfma_i32_16x16x64_i8 v[98:101], v[216:219], v[242:245], v[98:101]
	v_mfma_i32_16x16x64_i8 v[86:89], v[208:211], v[250:253], v[86:89]
	v_mfma_i32_16x16x64_i8 v[82:85], v[216:219], v[250:253], v[82:85]
	s_setprio 0
	s_barrier
	s_add_i32 s28, s41, s57
	v_lshl_add_u64 v[28:29], v[184:185], 0, s[24:25]
	s_mov_b32 m0, s28
	ds_read_b128 v[220:223], v224 offset:49152
	ds_read_b128 v[226:229], v224 offset:50176
	ds_read_b128 v[230:233], v224 offset:51200
	ds_read_b128 v[234:237], v224 offset:52224
	ds_read_b128 v[238:241], v224 offset:53248
	ds_read_b128 v[242:245], v224 offset:54272
	ds_read_b128 v[246:249], v224 offset:55296
	ds_read_b128 v[250:253], v224 offset:56320
	global_load_lds_dwordx4 v[28:29], off
	s_add_i32 m0, s28, 0x2000
	s_add_u32 s28, s46, 0x40080
	v_lshl_add_u64 v[28:29], v[188:189], 0, s[24:25]
	s_addc_u32 s29, s47, 0
	s_add_i32 s41, s50, s57
	global_load_lds_dwordx4 v[28:29], off
	v_lshl_add_u64 v[28:29], s[28:29], 0, v[148:149]
	s_mov_b32 m0, s41
	s_nop 0
	global_load_lds_dwordx4 v[28:29], off
	v_lshl_add_u64 v[28:29], s[28:29], 0, v[152:153]
	s_add_i32 m0, s41, 0x2000
	s_nop 0
	global_load_lds_dwordx4 v[28:29], off
	v_lshl_add_u64 v[28:29], v[192:193], 0, s[24:25]
	s_mov_b32 m0, s64
	s_nop 0
	global_load_lds_dwordx4 v[28:29], off
	v_lshl_add_u64 v[28:29], v[200:201], 0, s[24:25]
	s_mov_b32 m0, s65
	s_nop 0
	global_load_lds_dwordx4 v[28:29], off
	s_waitcnt vmcnt(8)
	s_and_b64 vcc, exec, s[26:27]
	s_cbranch_vccnz .Lnl_4
	s_waitcnt lgkmcnt(0)
.Lnl_4:
	s_barrier
	s_setprio 1
	s_waitcnt lgkmcnt(0)
	v_mfma_i32_16x16x64_i8 v[78:81], v[54:57], v[220:223], v[78:81]
	v_mfma_i32_16x16x64_i8 v[74:77], v[70:73], v[220:223], v[74:77]
	v_mfma_i32_16x16x64_i8 v[62:65], v[54:57], v[230:233], v[62:65]
	v_mfma_i32_16x16x64_i8 v[58:61], v[70:73], v[230:233], v[58:61]
	v_mfma_i32_16x16x64_i8 v[46:49], v[54:57], v[238:241], v[46:49]
	v_mfma_i32_16x16x64_i8 v[42:45], v[70:73], v[238:241], v[42:45]
	v_mfma_i32_16x16x64_i8 v[14:17], v[54:57], v[246:249], v[14:17]
	v_mfma_i32_16x16x64_i8 v[10:13], v[70:73], v[246:249], v[10:13]
	v_mfma_i32_16x16x64_i8 v[78:81], v[66:69], v[226:229], v[78:81]
	v_mfma_i32_16x16x64_i8 v[74:77], v[178:181], v[226:229], v[74:77]
	v_mfma_i32_16x16x64_i8 v[62:65], v[66:69], v[234:237], v[62:65]
	v_mfma_i32_16x16x64_i8 v[58:61], v[178:181], v[234:237], v[58:61]
	v_mfma_i32_16x16x64_i8 v[46:49], v[66:69], v[242:245], v[46:49]
	v_mfma_i32_16x16x64_i8 v[42:45], v[178:181], v[242:245], v[42:45]
	v_mfma_i32_16x16x64_i8 v[14:17], v[66:69], v[250:253], v[14:17]
	v_mfma_i32_16x16x64_i8 v[10:13], v[178:181], v[250:253], v[10:13]
	s_setprio 0
	s_setprio 1
	v_mfma_i32_16x16x64_i8 v[20:23], v[196:199], v[220:223], v[20:23]
	v_mfma_i32_16x16x64_i8 v[70:73], v[208:211], v[226:229], v[20:23]
	v_mfma_i32_16x16x64_i8 v[20:23], v[212:215], v[220:223], v[34:37]
	v_mfma_i32_16x16x64_i8 v[66:69], v[216:219], v[226:229], v[20:23]
	v_mfma_i32_16x16x64_i8 v[20:23], v[196:199], v[230:233], v[38:41]
	v_mfma_i32_16x16x64_i8 v[54:57], v[208:211], v[234:237], v[20:23]
	v_mfma_i32_16x16x64_i8 v[20:23], v[212:215], v[230:233], v[50:53]
	v_mfma_i32_16x16x64_i8 v[50:53], v[216:219], v[234:237], v[20:23]
	v_mfma_i32_16x16x64_i8 v[20:23], v[196:199], v[238:241], v[30:33]
	v_mfma_i32_16x16x64_i8 v[30:33], v[208:211], v[242:245], v[20:23]
	v_mfma_i32_16x16x64_i8 v[20:23], v[212:215], v[238:241], v[24:27]
	v_mfma_i32_16x16x64_i8 v[6:9], v[196:199], v[246:249], v[6:9]
	v_mfma_i32_16x16x64_i8 v[2:5], v[212:215], v[246:249], v[2:5]
	v_mfma_i32_16x16x64_i8 v[26:29], v[216:219], v[242:245], v[20:23]
	v_mfma_i32_16x16x64_i8 v[6:9], v[208:211], v[250:253], v[6:9]
	v_mfma_i32_16x16x64_i8 v[2:5], v[216:219], v[250:253], v[2:5]
	s_setprio 0
	s_barrier
	s_add_i32 s39, s39, 2
	s_add_u32 s10, s10, 0x100
	s_addc_u32 s11, s11, 0
	s_add_u32 s20, s20, 0x100
	s_addc_u32 s33, s33, 0
	s_cmp_gt_u32 s39, 13
	s_cbranch_scc0 .LBB0_238
	s_and_b64 vcc, exec, s[26:27]
	s_cbranch_vccz .LBB0_241
	s_barrier
